# hybrid K1 ring 16 (16KiB chunks, 14 private + queues) + flush spread over the stream
# baseline (speedup 1.0000x reference)
.Lk1_scan:
	s_load_dwordx2 s[4:5], s[0:1], 0x0
	s_load_dwordx4 s[8:11], s[0:1], 0x20
	s_load_dwordx2 s[12:13], s[0:1], 0x30
	v_and_b32_e32 v6, 63, v0
	v_readfirstlane_b32 s3, v0
	v_lshlrev_b32_e32 v1, 4, v6
	v_lshlrev_b32_e32 v2, 2, v6
	v_or_b32_e32 v3, 1, v2
	v_or_b32_e32 v4, 2, v2
	v_or_b32_e32 v5, 3, v2
	s_lshr_b32 s3, s3, 6
	s_sub_u32 s16, s2, 0x60
	s_lshl_b32 s16, s16, 2
	s_add_u32 s16, s16, s3
	s_mul_i32 s17, s16, 0x48000
	s_lshr_b32 s18, s17, 2
	s_lshl_b32 s24, s3, 13
	s_mov_b32 s25, s24
	s_mov_b32 s28, s24
	s_mov_b32 s36, 0
	v_mov_b32_e32 v21, 1
	s_mov_b32 s27, 0
	s_mov_b32 s29, 0x55555556
	s_mov_b32 s31, 0xc0000
	s_waitcnt lgkmcnt(0)
	s_and_b32 s50, s16, 15
	s_mul_i32 s52, s50, 512
	s_add_u32 s52, s52, 28672
	s_lshl_b32 s53, s50, 6
	s_add_u32 s53, s53, 0xe000
	s_add_u32 s54, s10, s53
	s_addc_u32 s55, s11, 0
	s_mul_i32 s59, s16, 14
	s_mul_i32 s57, s59, 0x4000
	s_lshr_b32 s18, s57, 2
	s_add_u32 s6, s4, s57
	s_addc_u32 s7, s5, 0
	v_mov_b32_e32 v27, 0
	global_load_dwordx4 v[28:31], v1, s[6:7] nt
	s_add_u32 s6, s6, 0x400
	s_addc_u32 s7, s7, 0
	global_load_dwordx4 v[32:35], v1, s[6:7] nt
	s_add_u32 s6, s6, 0x400
	s_addc_u32 s7, s7, 0
	global_load_dwordx4 v[36:39], v1, s[6:7] nt
	s_add_u32 s6, s6, 0x400
	s_addc_u32 s7, s7, 0
	global_load_dwordx4 v[40:43], v1, s[6:7] nt
	s_add_u32 s6, s6, 0x400
	s_addc_u32 s7, s7, 0
	global_load_dwordx4 v[44:47], v1, s[6:7] nt
	s_add_u32 s6, s6, 0x400
	s_addc_u32 s7, s7, 0
	global_load_dwordx4 v[48:51], v1, s[6:7] nt
	s_add_u32 s6, s6, 0x400
	s_addc_u32 s7, s7, 0
	global_load_dwordx4 v[52:55], v1, s[6:7] nt
	s_add_u32 s6, s6, 0x400
	s_addc_u32 s7, s7, 0
	global_load_dwordx4 v[56:59], v1, s[6:7] nt
	s_add_u32 s6, s6, 0x400
	s_addc_u32 s7, s7, 0
	global_load_dwordx4 v[60:63], v1, s[6:7] nt
	s_add_u32 s6, s6, 0x400
	s_addc_u32 s7, s7, 0
	global_load_dwordx4 v[64:67], v1, s[6:7] nt
	s_add_u32 s6, s6, 0x400
	s_addc_u32 s7, s7, 0
	global_load_dwordx4 v[68:71], v1, s[6:7] nt
	s_add_u32 s6, s6, 0x400
	s_addc_u32 s7, s7, 0
	global_load_dwordx4 v[72:75], v1, s[6:7] nt
	s_add_u32 s6, s6, 0x400
	s_addc_u32 s7, s7, 0
	global_load_dwordx4 v[76:79], v1, s[6:7] nt
	s_add_u32 s6, s6, 0x400
	s_addc_u32 s7, s7, 0
	global_load_dwordx4 v[80:83], v1, s[6:7] nt
	s_add_u32 s6, s6, 0x400
	s_addc_u32 s7, s7, 0
	global_load_dwordx4 v[84:87], v1, s[6:7] nt
	s_add_u32 s6, s6, 0x400
	s_addc_u32 s7, s7, 0
	global_load_dwordx4 v[88:91], v1, s[6:7] nt
	s_add_u32 s6, s6, 0x400
	s_addc_u32 s7, s7, 0
	s_mov_b32 s26, 18
	s_add_u32 s57, s59, 1
	s_mul_i32 s57, s57, 0x4000
	s_lshr_b32 s58, s57, 2
	s_add_u32 s6, s4, s57
	s_addc_u32 s7, s5, 0
	s_mov_b32 s26, 0

.Lk1_contm_15:
	global_load_dwordx4 v[60:63], v1, s[6:7] nt
	s_add_u32 s6, s6, 0x400
	s_addc_u32 s7, s7, 0
	global_load_dwordx4 v[64:67], v1, s[6:7] nt
	s_add_u32 s6, s6, 0x400
	s_addc_u32 s7, s7, 0
	global_load_dwordx4 v[68:71], v1, s[6:7] nt
	s_add_u32 s6, s6, 0x400
	s_addc_u32 s7, s7, 0
	global_load_dwordx4 v[72:75], v1, s[6:7] nt
	s_add_u32 s6, s6, 0x400
	s_addc_u32 s7, s7, 0
	global_load_dwordx4 v[76:79], v1, s[6:7] nt
	s_add_u32 s6, s6, 0x400
	s_addc_u32 s7, s7, 0
	global_load_dwordx4 v[80:83], v1, s[6:7] nt
	s_add_u32 s6, s6, 0x400
	s_addc_u32 s7, s7, 0
	global_load_dwordx4 v[84:87], v1, s[6:7] nt
	s_add_u32 s6, s6, 0x400
	s_addc_u32 s7, s7, 0
	global_load_dwordx4 v[88:91], v1, s[6:7] nt
	s_add_u32 s6, s6, 0x400
	s_addc_u32 s7, s7, 0
	s_mov_b32 s18, s58
	s_add_u32 s60, s26, 2
	s_cmp_lt_u32 s60, 14
	s_cbranch_scc0 .Lk1_dynid
	s_add_u32 s57, s59, s60
	s_branch .Lk1_haveid
.Lk1_dynid:
	v_readfirstlane_b32 s56, v26
	s_nop 0
	s_cmp_lt_u32 s56, 512
	s_cbranch_scc0 .Lk1_lastchunk
	s_add_u32 s57, s52, s56
.Lk1_haveid:
	s_mul_i32 s57, s57, 0x4000
	s_lshr_b32 s58, s57, 2
	s_add_u32 s6, s4, s57
	s_addc_u32 s7, s5, 0
	s_add_u32 s60, s26, 3
	s_cmp_lt_u32 s60, 14
	s_cbranch_scc1 .Lk1_noreq
	s_mov_b64 exec, 1
	global_atomic_add v26, v27, v21, s[54:55] sc0
	s_mov_b64 exec, -1
